# speedup vs baseline: 1.0013x; 1.0000x over previous
.LBB0_24:
	s_ashr_i32 s6, s2, 3
	s_and_b32 s3, s2, 4
	s_and_b32 s6, s6, -8
	s_or_b32 s33, s6, s3
	s_lshl_b32 s3, s2, 3
	s_and_b32 s3, s3, 24
	s_bfe_u32 s2, s2, 0x30003
	s_load_dwordx2 s[4:5], s[0:1], 0x0
	s_load_dwordx4 s[36:39], s[0:1], 0x10
	s_or_b32 s6, s3, s2
	s_lshl_b32 s2, s33, 7
	s_lshl_b32 s40, s6, 4
	s_or_b32 s2, s2, s40
	s_ashr_i32 s3, s2, 31
	s_lshl_b64 s[2:3], s[2:3], 12
	s_waitcnt lgkmcnt(0)
	s_add_u32 s0, s4, s2
	s_addc_u32 s1, s5, s3
	v_lshlrev_b32_e32 v66, 4, v0
	v_mov_b32_e32 v67, 0
	v_lshl_add_u64 v[2:3], s[0:1], 0, v[66:67]
	global_load_dwordx4 v[62:65], v66, s[0:1] nt
	s_movk_i32 s0, 0x2000
	v_add_co_u32_e32 v4, vcc, s0, v2
	s_movk_i32 s0, 0x4000
	s_nop 0
	v_addc_co_u32_e32 v5, vcc, 0, v3, vcc
	global_load_dwordx4 v[58:61], v[4:5], off offset:-4096 nt
	global_load_dwordx4 v[54:57], v[4:5], off nt
	v_add_co_u32_e32 v4, vcc, s0, v2
	s_movk_i32 s0, 0x6000
	s_nop 0
	v_addc_co_u32_e32 v5, vcc, 0, v3, vcc
	global_load_dwordx4 v[50:53], v[4:5], off offset:-4096 nt
	global_load_dwordx4 v[46:49], v[4:5], off nt
	v_add_co_u32_e32 v4, vcc, s0, v2
	s_mov_b32 s0, 0x8000
	s_nop 0
	v_addc_co_u32_e32 v5, vcc, 0, v3, vcc
	global_load_dwordx4 v[42:45], v[4:5], off offset:-4096 nt
	global_load_dwordx4 v[38:41], v[4:5], off nt
	v_add_co_u32_e32 v4, vcc, s0, v2
	s_mov_b32 s0, 0xa000
	s_nop 0
	v_addc_co_u32_e32 v5, vcc, 0, v3, vcc
	global_load_dwordx4 v[34:37], v[4:5], off offset:-4096 nt
	global_load_dwordx4 v[30:33], v[4:5], off nt
	v_add_co_u32_e32 v4, vcc, s0, v2
	s_mov_b32 s0, 0xc000
	s_nop 0
	v_addc_co_u32_e32 v5, vcc, 0, v3, vcc
	global_load_dwordx4 v[26:29], v[4:5], off offset:-4096 nt
	global_load_dwordx4 v[22:25], v[4:5], off nt
	v_add_co_u32_e32 v4, vcc, s0, v2
	s_mov_b32 s0, 0xe000
	s_nop 0
	v_addc_co_u32_e32 v5, vcc, 0, v3, vcc
	global_load_dwordx4 v[18:21], v[4:5], off offset:-4096 nt
	global_load_dwordx4 v[14:17], v[4:5], off nt
	v_add_co_u32_e32 v4, vcc, s0, v2
	s_mov_b32 s0, 0xf000
	s_nop 0
	v_addc_co_u32_e32 v5, vcc, 0, v3, vcc
	global_load_dwordx4 v[10:13], v[4:5], off offset:-4096 nt
	global_load_dwordx4 v[6:9], v[4:5], off nt
	v_add_co_u32_e32 v2, vcc, s0, v2
	s_lshl_b32 s41, s6, 6
	s_nop 0
	v_addc_co_u32_e32 v3, vcc, 0, v3, vcc
	global_load_dwordx4 v[2:5], v[2:3], off nt
	s_load_dwordx16 s[0:15], s[36:37], s41 offset:0x0
	s_load_dwordx16 s[16:31], s[38:39], s41 offset:0x0
	s_waitcnt lgkmcnt(0)
	s_waitcnt vmcnt(15)
	v_add_f32_e32 v1, v62, v63
	v_add_f32_e32 v66, v64, v65
	v_add_f32_e32 v1, v1, v66
	v_add_f32_e32 v1, 0, v1
	s_waitcnt vmcnt(14)
	v_add_f32_e32 v66, v58, v59
	v_add_f32_e32 v68, v60, v61
	s_waitcnt vmcnt(13)
	v_add_f32_e32 v69, v54, v55
	v_add_f32_e32 v70, v56, v57
	v_add_f32_e32 v66, v66, v68
	v_add_f32_e32 v69, v69, v70
	s_waitcnt vmcnt(12)
	v_add_f32_e32 v71, v50, v51
	v_add_f32_e32 v72, v52, v53
	v_add_f32_e32 v1, v1, v66
	s_waitcnt vmcnt(11)
	v_add_f32_e32 v73, v46, v47
	v_add_f32_e32 v74, v48, v49
	v_add_f32_e32 v71, v71, v72
	v_add_f32_e32 v1, v1, v69
	s_waitcnt vmcnt(10)
	v_add_f32_e32 v68, v42, v43
	v_add_f32_e32 v70, v44, v45
	v_add_f32_e32 v72, v73, v74
	v_add_f32_e32 v1, v1, v71
	s_waitcnt vmcnt(9)
	v_add_f32_e32 v73, v38, v39
	v_add_f32_e32 v68, v68, v70
	v_add_f32_e32 v70, v40, v41
	v_add_f32_e32 v1, v1, v72
	v_add_f32_e32 v70, v73, v70
	s_waitcnt vmcnt(8)
	v_add_f32_e32 v66, v34, v35
	v_add_f32_e32 v1, v1, v68
	v_add_f32_e32 v68, v36, v37
	v_add_f32_e32 v1, v1, v70
	v_add_f32_e32 v66, v66, v68
	v_add_f32_e32 v1, v1, v66
	s_waitcnt vmcnt(7)
	v_add_f32_e32 v66, v30, v31
	v_add_f32_e32 v68, v32, v33
	v_add_f32_e32 v66, v66, v68
	v_add_f32_e32 v1, v1, v66
	s_waitcnt vmcnt(6)
	v_add_f32_e32 v66, v26, v27
	v_add_f32_e32 v68, v28, v29
	v_add_f32_e32 v66, v66, v68
	v_add_f32_e32 v1, v1, v66
	s_waitcnt vmcnt(5)
	v_add_f32_e32 v66, v22, v23
	v_add_f32_e32 v68, v24, v25
	v_add_f32_e32 v66, v66, v68
	v_add_f32_e32 v1, v1, v66
	s_waitcnt vmcnt(4)
	v_add_f32_e32 v66, v18, v19
	v_add_f32_e32 v68, v20, v21
	v_add_f32_e32 v66, v66, v68
	v_add_f32_e32 v1, v1, v66
	s_waitcnt vmcnt(3)
	v_add_f32_e32 v66, v14, v15
	v_add_f32_e32 v68, v16, v17
	v_add_f32_e32 v66, v66, v68
	v_add_f32_e32 v1, v1, v66
	s_waitcnt vmcnt(2)
	v_add_f32_e32 v66, v10, v11
	v_add_f32_e32 v68, v12, v13
	v_add_f32_e32 v66, v66, v68
	v_add_f32_e32 v1, v1, v66
	s_waitcnt vmcnt(1)
	v_add_f32_e32 v66, v6, v7
	v_add_f32_e32 v68, v8, v9
	v_add_f32_e32 v66, v66, v68
	v_add_f32_e32 v1, v1, v66
	s_waitcnt vmcnt(0)
	v_add_f32_e32 v66, v2, v3
	v_add_f32_e32 v68, v4, v5
	v_add_f32_e32 v66, v66, v68
	v_add_f32_e32 v66, v1, v66
	v_mov_b32_e32 v68, v66
	s_nop 1
	v_permlane32_swap_b32_e32 v68, v66
	v_add_f32_e32 v66, v68, v66
	v_mov_b32_e32 v68, v66
	s_nop 1
	v_permlane16_swap_b32_e32 v68, v66
	v_add_f32_e32 v66, v68, v66
	s_nop 1
	v_add_f32_dpp v66, v66, v66 row_ror:8 row_mask:0xf bank_mask:0xf
	s_nop 1
	v_mov_b32_dpp v68, v66 row_half_mirror row_mask:0xf bank_mask:0xf
	s_nop 1
	v_add_f32_dpp v66, v68, v66 quad_perm:[3,2,1,0] row_mask:0xf bank_mask:0xf
	s_nop 1
	v_add_f32_dpp v66, v66, v66 quad_perm:[2,3,0,1] row_mask:0xf bank_mask:0xf
	s_nop 1
	v_add_f32_dpp v73, v66, v66 quad_perm:[1,0,3,2] row_mask:0xf bank_mask:0xf
	v_and_b32_e32 v72, 63, v0
	v_lshrrev_b32_e32 v71, 4, v0
	v_cmp_eq_u32_e32 vcc, 0, v72
	s_and_saveexec_b64 s[36:37], vcc
	s_cbranch_execz .LBB0_26
	ds_write_b32 v71, v73
.LBB0_26:
	s_or_b64 exec, exec, s[36:37]
	s_waitcnt lgkmcnt(0)
	s_barrier
	ds_read_b128 v[74:77], v67
	s_waitcnt lgkmcnt(0)
	v_add_f32_e32 v67, v74, v75
	v_add_f32_e32 v67, v67, v76
	v_add_f32_e32 v73, v67, v77
	v_fmamk_f32 v74, v73, 0xb8800000, v63
	v_fmamk_f32 v67, v73, 0xb8800000, v62
	v_fmamk_f32 v76, v73, 0xb8800000, v65
	v_mul_f32_e32 v74, v74, v74
	v_fmamk_f32 v75, v73, 0xb8800000, v64
	v_fmac_f32_e32 v74, v67, v67
	v_mul_f32_e32 v67, v76, v76
	v_fmac_f32_e32 v67, v75, v75
	v_fmamk_f32 v75, v73, 0xb8800000, v59
	v_add_f32_e32 v67, v74, v67
	v_fmamk_f32 v74, v73, 0xb8800000, v58
	v_fmamk_f32 v77, v73, 0xb8800000, v61
	v_mul_f32_e32 v75, v75, v75
	v_fmamk_f32 v76, v73, 0xb8800000, v60
	v_fmac_f32_e32 v75, v74, v74
	v_mul_f32_e32 v74, v77, v77
	v_fmac_f32_e32 v74, v76, v76
	v_add_f32_e32 v74, v75, v74
	v_fmamk_f32 v75, v73, 0xb8800000, v55
	v_add_f32_e32 v67, v67, v74
	v_fmamk_f32 v74, v73, 0xb8800000, v54
	v_fmamk_f32 v77, v73, 0xb8800000, v57
	v_mul_f32_e32 v75, v75, v75
	v_fmamk_f32 v76, v73, 0xb8800000, v56
	v_fmac_f32_e32 v75, v74, v74
	v_mul_f32_e32 v74, v77, v77
	v_fmac_f32_e32 v74, v76, v76
	v_add_f32_e32 v74, v75, v74
	v_fmamk_f32 v75, v73, 0xb8800000, v51
	v_add_f32_e32 v67, v67, v74
	v_fmamk_f32 v74, v73, 0xb8800000, v50
	v_fmamk_f32 v77, v73, 0xb8800000, v53
	v_mul_f32_e32 v75, v75, v75
	v_fmamk_f32 v76, v73, 0xb8800000, v52
	v_fmac_f32_e32 v75, v74, v74
	v_mul_f32_e32 v74, v77, v77
	v_fmac_f32_e32 v74, v76, v76
	v_add_f32_e32 v74, v75, v74
	v_fmamk_f32 v75, v73, 0xb8800000, v47
	v_add_f32_e32 v67, v67, v74
	v_fmamk_f32 v74, v73, 0xb8800000, v46
	v_fmamk_f32 v77, v73, 0xb8800000, v49
	v_mul_f32_e32 v75, v75, v75
	v_fmamk_f32 v76, v73, 0xb8800000, v48
	v_fmac_f32_e32 v75, v74, v74
	v_mul_f32_e32 v74, v77, v77
	v_fmac_f32_e32 v74, v76, v76
	v_add_f32_e32 v74, v75, v74
	v_fmamk_f32 v75, v73, 0xb8800000, v43
	v_add_f32_e32 v67, v67, v74
	v_fmamk_f32 v74, v73, 0xb8800000, v42
	v_fmamk_f32 v77, v73, 0xb8800000, v45
	v_mul_f32_e32 v75, v75, v75
	v_fmamk_f32 v76, v73, 0xb8800000, v44
	v_fmac_f32_e32 v75, v74, v74
	v_mul_f32_e32 v74, v77, v77
	v_fmac_f32_e32 v74, v76, v76
	v_add_f32_e32 v74, v75, v74
	v_fmamk_f32 v75, v73, 0xb8800000, v39
	v_add_f32_e32 v67, v67, v74
	v_fmamk_f32 v74, v73, 0xb8800000, v38
	v_fmamk_f32 v77, v73, 0xb8800000, v41
	v_mul_f32_e32 v75, v75, v75
	v_fmamk_f32 v76, v73, 0xb8800000, v40
	v_fmac_f32_e32 v75, v74, v74
	v_mul_f32_e32 v74, v77, v77
	v_fmac_f32_e32 v74, v76, v76
	v_add_f32_e32 v74, v75, v74
	v_fmamk_f32 v75, v73, 0xb8800000, v35
	v_add_f32_e32 v67, v67, v74
	v_fmamk_f32 v74, v73, 0xb8800000, v34
	v_fmamk_f32 v77, v73, 0xb8800000, v37
	v_mul_f32_e32 v75, v75, v75
	v_fmamk_f32 v76, v73, 0xb8800000, v36
	v_fmac_f32_e32 v75, v74, v74
	v_mul_f32_e32 v74, v77, v77
	v_fmac_f32_e32 v74, v76, v76
	v_add_f32_e32 v74, v75, v74
	v_fmamk_f32 v75, v73, 0xb8800000, v31
	v_add_f32_e32 v67, v67, v74
	v_fmamk_f32 v74, v73, 0xb8800000, v30
	v_fmamk_f32 v77, v73, 0xb8800000, v33
	v_mul_f32_e32 v75, v75, v75
	v_fmamk_f32 v76, v73, 0xb8800000, v32
	v_fmac_f32_e32 v75, v74, v74
	v_mul_f32_e32 v74, v77, v77
	v_fmac_f32_e32 v74, v76, v76
	v_add_f32_e32 v74, v75, v74
	v_fmamk_f32 v75, v73, 0xb8800000, v27
	v_add_f32_e32 v67, v67, v74
	v_fmamk_f32 v74, v73, 0xb8800000, v26
	v_fmamk_f32 v77, v73, 0xb8800000, v29
	v_mul_f32_e32 v75, v75, v75
	v_fmamk_f32 v76, v73, 0xb8800000, v28
	v_fmac_f32_e32 v75, v74, v74
	v_mul_f32_e32 v74, v77, v77
	v_fmac_f32_e32 v74, v76, v76
	v_add_f32_e32 v74, v75, v74
	v_fmamk_f32 v75, v73, 0xb8800000, v23
	v_add_f32_e32 v67, v67, v74
	v_fmamk_f32 v74, v73, 0xb8800000, v22
	v_fmamk_f32 v77, v73, 0xb8800000, v25
	v_mul_f32_e32 v75, v75, v75
	v_fmamk_f32 v76, v73, 0xb8800000, v24
	v_fmac_f32_e32 v75, v74, v74
	v_mul_f32_e32 v74, v77, v77
	v_fmac_f32_e32 v74, v76, v76
	v_add_f32_e32 v74, v75, v74
	v_fmamk_f32 v75, v73, 0xb8800000, v19
	v_add_f32_e32 v67, v67, v74
	v_fmamk_f32 v74, v73, 0xb8800000, v18
	v_fmamk_f32 v77, v73, 0xb8800000, v21
	v_mul_f32_e32 v75, v75, v75
	v_fmamk_f32 v76, v73, 0xb8800000, v20
	v_fmac_f32_e32 v75, v74, v74
	v_mul_f32_e32 v74, v77, v77
	v_fmac_f32_e32 v74, v76, v76
	v_add_f32_e32 v74, v75, v74
	v_fmamk_f32 v75, v73, 0xb8800000, v15
	v_add_f32_e32 v67, v67, v74
	v_fmamk_f32 v74, v73, 0xb8800000, v14
	v_fmamk_f32 v77, v73, 0xb8800000, v17
	v_mul_f32_e32 v75, v75, v75
	v_fmamk_f32 v76, v73, 0xb8800000, v16
	v_fmac_f32_e32 v75, v74, v74
	v_mul_f32_e32 v74, v77, v77
	v_fmac_f32_e32 v74, v76, v76
	v_add_f32_e32 v74, v75, v74
	v_fmamk_f32 v75, v73, 0xb8800000, v11
	v_add_f32_e32 v67, v67, v74
	v_fmamk_f32 v74, v73, 0xb8800000, v10
	v_fmamk_f32 v77, v73, 0xb8800000, v13
	v_mul_f32_e32 v75, v75, v75
	v_fmamk_f32 v76, v73, 0xb8800000, v12
	v_fmac_f32_e32 v75, v74, v74
	v_mul_f32_e32 v74, v77, v77
	v_fmac_f32_e32 v74, v76, v76
	v_add_f32_e32 v74, v75, v74
	v_fmamk_f32 v75, v73, 0xb8800000, v7
	v_add_f32_e32 v67, v67, v74
	v_fmamk_f32 v74, v73, 0xb8800000, v6
	v_fmamk_f32 v77, v73, 0xb8800000, v9
	v_mul_f32_e32 v75, v75, v75
	v_fmamk_f32 v76, v73, 0xb8800000, v8
	v_fmac_f32_e32 v75, v74, v74
	v_mul_f32_e32 v74, v77, v77
	v_fmac_f32_e32 v74, v76, v76
	v_add_f32_e32 v74, v75, v74
	v_fmamk_f32 v75, v73, 0xb8800000, v3
	v_add_f32_e32 v67, v67, v74
	v_fmamk_f32 v74, v73, 0xb8800000, v2
	v_fmamk_f32 v77, v73, 0xb8800000, v5
	v_mul_f32_e32 v75, v75, v75
	v_fmamk_f32 v76, v73, 0xb8800000, v4
	v_fmac_f32_e32 v75, v74, v74
	v_mul_f32_e32 v74, v77, v77
	v_fmac_f32_e32 v74, v76, v76
	v_add_f32_e32 v74, v75, v74
	v_add_f32_e32 v67, v67, v74
	v_mov_b32_e32 v66, v67
	s_nop 1
	v_permlane32_swap_b32_e32 v66, v67
	v_add_f32_e32 v67, v66, v67
	v_mov_b32_e32 v66, v67
	s_nop 1
	v_permlane16_swap_b32_e32 v66, v67
	v_add_f32_e32 v67, v66, v67
	s_nop 1
	v_add_f32_dpp v67, v67, v67 row_ror:8 row_mask:0xf bank_mask:0xf
	s_nop 1
	v_mov_b32_dpp v66, v67 row_half_mirror row_mask:0xf bank_mask:0xf
	s_nop 1
	v_add_f32_dpp v67, v66, v67 quad_perm:[3,2,1,0] row_mask:0xf bank_mask:0xf
	s_nop 1
	v_add_f32_dpp v67, v67, v67 quad_perm:[2,3,0,1] row_mask:0xf bank_mask:0xf
	s_nop 1
	v_add_f32_dpp v66, v67, v67 quad_perm:[1,0,3,2] row_mask:0xf bank_mask:0xf
	v_mul_f32_e32 v1, 0x38800000, v73
	s_and_saveexec_b64 s[36:37], vcc
	s_cbranch_execz .LBB0_28
	ds_write_b32 v71, v66 offset:16
